# v45 + loop-edge edit in G1 K-loop: fragment reads issued ahead of the scalar address block at the back edge; half-unit ballot replaced by its mask
# speedup vs baseline: 1.0055x; 1.0055x over previous
.LBB0_514:
	v_add_u32_e32 v130, 0x10000, v223
	v_add_u32_e32 v142, 0x14000, v223
	ds_read_b128 v[146:149], v130
	ds_read_b128 v[150:153], v130 offset:1024
	ds_read_b128 v[154:157], v130 offset:2048
	ds_read_b128 v[158:161], v130 offset:3072
	ds_read_b128 v[130:133], v142
	ds_read_b128 v[134:137], v142 offset:1024
	ds_read_b128 v[138:141], v142 offset:2048
	ds_read_b128 v[142:145], v142 offset:3072
	ds_read_b128 v[162:165], v224
	ds_read_b128 v[166:169], v224 offset:1024
	ds_read_b128 v[170:173], v224 offset:2048
	ds_read_b128 v[174:177], v224 offset:3072
	ds_read_b128 v[178:181], v224 offset:4096
	ds_read_b128 v[182:185], v224 offset:5120
	ds_read_b128 v[186:189], v224 offset:6144
	ds_read_b128 v[190:193], v224 offset:7168
	s_add_u32 s22, s82, s92
	s_addc_u32 s23, s83, s93
	s_add_u32 s24, s22, 0x100
	s_addc_u32 s25, s23, 0
	s_add_u32 s58, s3, s92
	s_addc_u32 s59, s2, s93
	s_add_i32 vcc_lo, 0, 0x10000
	s_cmpk_eq_i32 s92, 0xf00
	s_cselect_b64 s[26:27], -1, 0
	s_and_b64 s[22:23], s[26:27], exec
	s_cselect_b32 s25, s67, s25
	s_cselect_b32 s24, s75, s24
	s_cselect_b32 s23, s95, s59
	s_cselect_b32 s22, s29, s58
	s_add_i32 vcc_hi, 0, 0x14000
	v_lshl_add_u64 v[214:215], v[210:211], 0, s[92:93]
	s_add_i32 m0, s81, 0xc000
	s_nop 0
	global_load_lds_dwordx4 v[214:215], off
	v_lshl_add_u64 v[214:215], v[212:213], 0, s[92:93]
	s_add_i32 m0, s81, 0xe000
	s_nop 0
	global_load_lds_dwordx4 v[214:215], off
	s_waitcnt vmcnt(8)
	s_waitcnt lgkmcnt(0)
	s_barrier
	v_mfma_f32_16x16x32_bf16 v[124:127], v[146:149], v[162:165], v[124:127]
	v_mfma_f32_16x16x32_bf16 v[120:123], v[154:157], v[162:165], v[120:123]
	v_mfma_f32_16x16x32_bf16 v[116:119], v[146:149], v[170:173], v[116:119]
	v_mfma_f32_16x16x32_bf16 v[108:111], v[154:157], v[170:173], v[108:111]
	v_mfma_f32_16x16x32_bf16 v[100:103], v[146:149], v[178:181], v[100:103]
	v_mfma_f32_16x16x32_bf16 v[92:95], v[154:157], v[178:181], v[92:95]
	v_mfma_f32_16x16x32_bf16 v[84:87], v[146:149], v[186:189], v[84:87]
	v_mfma_f32_16x16x32_bf16 v[76:79], v[154:157], v[186:189], v[76:79]
	v_mfma_f32_16x16x32_bf16 v[124:127], v[150:153], v[166:169], v[124:127]
	v_mfma_f32_16x16x32_bf16 v[120:123], v[158:161], v[166:169], v[120:123]
	v_mfma_f32_16x16x32_bf16 v[116:119], v[150:153], v[174:177], v[116:119]
	v_mfma_f32_16x16x32_bf16 v[108:111], v[158:161], v[174:177], v[108:111]
	v_mfma_f32_16x16x32_bf16 v[100:103], v[150:153], v[182:185], v[100:103]
	v_mfma_f32_16x16x32_bf16 v[92:95], v[158:161], v[182:185], v[92:95]
	v_mfma_f32_16x16x32_bf16 v[84:87], v[150:153], v[190:193], v[84:87]
	v_mfma_f32_16x16x32_bf16 v[76:79], v[158:161], v[190:193], v[76:79]
	v_mfma_f32_16x16x32_bf16 v[112:115], v[130:133], v[162:165], v[112:115]
	v_mfma_f32_16x16x32_bf16 v[104:107], v[138:141], v[162:165], v[104:107]
	v_mfma_f32_16x16x32_bf16 v[96:99], v[130:133], v[170:173], v[96:99]
	v_mfma_f32_16x16x32_bf16 v[88:91], v[138:141], v[170:173], v[88:91]
	v_mfma_f32_16x16x32_bf16 v[80:83], v[130:133], v[178:181], v[80:83]
	v_mfma_f32_16x16x32_bf16 v[72:75], v[138:141], v[178:181], v[72:75]
	v_mfma_f32_16x16x32_bf16 v[68:71], v[130:133], v[186:189], v[68:71]
	v_mfma_f32_16x16x32_bf16 v[64:67], v[138:141], v[186:189], v[64:67]
	v_mfma_f32_16x16x32_bf16 v[112:115], v[134:137], v[166:169], v[112:115]
	v_mfma_f32_16x16x32_bf16 v[104:107], v[142:145], v[166:169], v[104:107]
	v_mfma_f32_16x16x32_bf16 v[96:99], v[134:137], v[174:177], v[96:99]
	v_mfma_f32_16x16x32_bf16 v[88:91], v[142:145], v[174:177], v[88:91]
	v_mfma_f32_16x16x32_bf16 v[80:83], v[134:137], v[182:185], v[80:83]
	v_mfma_f32_16x16x32_bf16 v[72:75], v[142:145], v[182:185], v[72:75]
	v_mfma_f32_16x16x32_bf16 v[68:71], v[134:137], v[190:193], v[68:71]
	v_mfma_f32_16x16x32_bf16 v[64:67], v[142:145], v[190:193], v[64:67]
	s_barrier
	s_add_i32 s58, vcc_lo, s28
	v_lshl_add_u64 v[214:215], s[22:23], 0, v[200:201]
	s_mov_b32 m0, s58
	ds_read_b128 v[186:189], v224 offset:16384
	ds_read_b128 v[190:193], v224 offset:17408
	ds_read_b128 v[178:181], v224 offset:18432
	ds_read_b128 v[182:185], v224 offset:19456
	ds_read_b128 v[170:173], v224 offset:20480
	ds_read_b128 v[174:177], v224 offset:21504
	ds_read_b128 v[162:165], v224 offset:22528
	ds_read_b128 v[166:169], v224 offset:23552
	global_load_lds_dwordx4 v[214:215], off
	s_add_i32 m0, s58, 0x2000
	s_add_u32 s58, s22, 0x80000
	v_lshl_add_u64 v[216:217], s[22:23], 0, v[204:205]
	s_addc_u32 s59, s23, 0
	s_add_i32 vcc_lo, vcc_hi, s28
	global_load_lds_dwordx4 v[216:217], off
	v_lshl_add_u64 v[218:219], s[58:59], 0, v[200:201]
	s_mov_b32 m0, vcc_lo
	v_lshl_add_u64 v[220:221], s[24:25], 0, v[202:203]
	global_load_lds_dwordx4 v[218:219], off
	v_lshl_add_u64 v[218:219], s[58:59], 0, v[204:205]
	s_add_i32 m0, vcc_lo, 0x2000
	global_load_lds_dwordx4 v[218:219], off
	v_lshl_add_u64 v[218:219], s[24:25], 0, v[198:199]
	s_mov_b32 m0, s81
	global_load_lds_dwordx4 v[218:219], off
	s_mov_b32 m0, s88
	s_andn2_b64 vcc, exec, s[96:97]
	global_load_lds_dwordx4 v[220:221], off
	s_waitcnt vmcnt(8)
	s_waitcnt lgkmcnt(0)
	s_barrier
	s_cbranch_vccnz .LBB0_516
	s_waitcnt lgkmcnt(0)
	v_mfma_f32_16x16x32_bf16 v[60:63], v[146:149], v[186:189], v[60:63]
	v_mfma_f32_16x16x32_bf16 v[56:59], v[154:157], v[186:189], v[56:59]
	v_mfma_f32_16x16x32_bf16 v[44:47], v[146:149], v[178:181], v[44:47]
	v_mfma_f32_16x16x32_bf16 v[40:43], v[154:157], v[178:181], v[40:43]
	v_mfma_f32_16x16x32_bf16 v[28:31], v[146:149], v[170:173], v[28:31]
	v_mfma_f32_16x16x32_bf16 v[24:27], v[154:157], v[170:173], v[24:27]
	v_mfma_f32_16x16x32_bf16 v[12:15], v[146:149], v[162:165], v[12:15]
	v_mfma_f32_16x16x32_bf16 v[8:11], v[154:157], v[162:165], v[8:11]
	v_mfma_f32_16x16x32_bf16 v[60:63], v[150:153], v[190:193], v[60:63]
	v_mfma_f32_16x16x32_bf16 v[56:59], v[158:161], v[190:193], v[56:59]
	v_mfma_f32_16x16x32_bf16 v[44:47], v[150:153], v[182:185], v[44:47]
	v_mfma_f32_16x16x32_bf16 v[40:43], v[158:161], v[182:185], v[40:43]
	v_mfma_f32_16x16x32_bf16 v[28:31], v[150:153], v[174:177], v[28:31]
	v_mfma_f32_16x16x32_bf16 v[24:27], v[158:161], v[174:177], v[24:27]
	v_mfma_f32_16x16x32_bf16 v[12:15], v[150:153], v[166:169], v[12:15]
	v_mfma_f32_16x16x32_bf16 v[8:11], v[158:161], v[166:169], v[8:11]
	v_mfma_f32_16x16x32_bf16 v[52:55], v[130:133], v[186:189], v[52:55]
	v_mfma_f32_16x16x32_bf16 v[48:51], v[138:141], v[186:189], v[48:51]
	v_mfma_f32_16x16x32_bf16 v[36:39], v[130:133], v[178:181], v[36:39]
	v_mfma_f32_16x16x32_bf16 v[32:35], v[138:141], v[178:181], v[32:35]
	v_mfma_f32_16x16x32_bf16 v[20:23], v[130:133], v[170:173], v[20:23]
	v_mfma_f32_16x16x32_bf16 v[16:19], v[138:141], v[170:173], v[16:19]
	v_mfma_f32_16x16x32_bf16 v[4:7], v[130:133], v[162:165], v[4:7]
	v_mfma_f32_16x16x32_bf16 v[0:3], v[138:141], v[162:165], v[0:3]
	v_mfma_f32_16x16x32_bf16 v[52:55], v[134:137], v[190:193], v[52:55]
	v_mfma_f32_16x16x32_bf16 v[48:51], v[142:145], v[190:193], v[48:51]
	v_mfma_f32_16x16x32_bf16 v[36:39], v[134:137], v[182:185], v[36:39]
	v_mfma_f32_16x16x32_bf16 v[32:35], v[142:145], v[182:185], v[32:35]
	v_mfma_f32_16x16x32_bf16 v[20:23], v[134:137], v[174:177], v[20:23]
	v_mfma_f32_16x16x32_bf16 v[16:19], v[142:145], v[174:177], v[16:19]
	v_mfma_f32_16x16x32_bf16 v[4:7], v[134:137], v[166:169], v[4:7]
	v_mfma_f32_16x16x32_bf16 v[0:3], v[142:145], v[166:169], v[0:3]
.LBB0_516:
	s_barrier
	s_add_i32 vcc_lo, 0, 0x18000
	s_add_i32 vcc_hi, 0, 0x1c000
	v_add_u32_e32 v130, vcc_lo, v223
	v_add_u32_e32 v142, vcc_hi, v223
	ds_read_b128 v[146:149], v130
	ds_read_b128 v[150:153], v130 offset:1024
	ds_read_b128 v[154:157], v130 offset:2048
	ds_read_b128 v[158:161], v130 offset:3072
	ds_read_b128 v[130:133], v142
	ds_read_b128 v[134:137], v142 offset:1024
	ds_read_b128 v[138:141], v142 offset:2048
	ds_read_b128 v[142:145], v142 offset:3072
	s_and_b64 s[26:27], s[26:27], exec
	s_cselect_b32 s27, s72, s86
	s_cselect_b32 s26, 0, s87
	s_add_u32 s24, s24, s27
	s_addc_u32 s25, s25, s26
	s_mov_b32 m0, s89
	v_lshl_add_u64 v[226:227], s[24:25], 0, v[198:199]
	ds_read_b128 v[162:165], v224 offset:32768
	ds_read_b128 v[166:169], v224 offset:33792
	ds_read_b128 v[170:173], v224 offset:34816
	ds_read_b128 v[174:177], v224 offset:35840
	ds_read_b128 v[178:181], v224 offset:36864
	ds_read_b128 v[182:185], v224 offset:37888
	ds_read_b128 v[186:189], v224 offset:38912
	ds_read_b128 v[190:193], v224 offset:39936
	global_load_lds_dwordx4 v[226:227], off
	v_lshl_add_u64 v[226:227], s[24:25], 0, v[202:203]
	s_mov_b32 m0, s90
	s_nop 0
	global_load_lds_dwordx4 v[226:227], off
	s_waitcnt vmcnt(8)
	s_waitcnt lgkmcnt(0)
	s_barrier
	v_mfma_f32_16x16x32_bf16 v[124:127], v[146:149], v[162:165], v[124:127]
	v_mfma_f32_16x16x32_bf16 v[120:123], v[154:157], v[162:165], v[120:123]
	v_mfma_f32_16x16x32_bf16 v[116:119], v[146:149], v[170:173], v[116:119]
	v_mfma_f32_16x16x32_bf16 v[108:111], v[154:157], v[170:173], v[108:111]
	v_mfma_f32_16x16x32_bf16 v[100:103], v[146:149], v[178:181], v[100:103]
	v_mfma_f32_16x16x32_bf16 v[92:95], v[154:157], v[178:181], v[92:95]
	v_mfma_f32_16x16x32_bf16 v[84:87], v[146:149], v[186:189], v[84:87]
	v_mfma_f32_16x16x32_bf16 v[76:79], v[154:157], v[186:189], v[76:79]
	v_mfma_f32_16x16x32_bf16 v[124:127], v[150:153], v[166:169], v[124:127]
	v_mfma_f32_16x16x32_bf16 v[120:123], v[158:161], v[166:169], v[120:123]
	v_mfma_f32_16x16x32_bf16 v[116:119], v[150:153], v[174:177], v[116:119]
	v_mfma_f32_16x16x32_bf16 v[108:111], v[158:161], v[174:177], v[108:111]
	v_mfma_f32_16x16x32_bf16 v[100:103], v[150:153], v[182:185], v[100:103]
	v_mfma_f32_16x16x32_bf16 v[92:95], v[158:161], v[182:185], v[92:95]
	v_mfma_f32_16x16x32_bf16 v[84:87], v[150:153], v[190:193], v[84:87]
	v_mfma_f32_16x16x32_bf16 v[76:79], v[158:161], v[190:193], v[76:79]
	v_mfma_f32_16x16x32_bf16 v[112:115], v[130:133], v[162:165], v[112:115]
	v_mfma_f32_16x16x32_bf16 v[104:107], v[138:141], v[162:165], v[104:107]
	v_mfma_f32_16x16x32_bf16 v[96:99], v[130:133], v[170:173], v[96:99]
	v_mfma_f32_16x16x32_bf16 v[88:91], v[138:141], v[170:173], v[88:91]
	v_mfma_f32_16x16x32_bf16 v[80:83], v[130:133], v[178:181], v[80:83]
	v_mfma_f32_16x16x32_bf16 v[72:75], v[138:141], v[178:181], v[72:75]
	v_mfma_f32_16x16x32_bf16 v[68:71], v[130:133], v[186:189], v[68:71]
	v_mfma_f32_16x16x32_bf16 v[64:67], v[138:141], v[186:189], v[64:67]
	v_mfma_f32_16x16x32_bf16 v[112:115], v[134:137], v[166:169], v[112:115]
	v_mfma_f32_16x16x32_bf16 v[104:107], v[142:145], v[166:169], v[104:107]
	v_mfma_f32_16x16x32_bf16 v[96:99], v[134:137], v[174:177], v[96:99]
	v_mfma_f32_16x16x32_bf16 v[88:91], v[142:145], v[174:177], v[88:91]
	v_mfma_f32_16x16x32_bf16 v[80:83], v[134:137], v[182:185], v[80:83]
	v_mfma_f32_16x16x32_bf16 v[72:75], v[142:145], v[182:185], v[72:75]
	v_mfma_f32_16x16x32_bf16 v[68:71], v[134:137], v[190:193], v[68:71]
	v_mfma_f32_16x16x32_bf16 v[64:67], v[142:145], v[190:193], v[64:67]
	s_barrier
	s_add_i32 s24, vcc_lo, s28
	v_lshl_add_u64 v[214:215], v[214:215], 0, s[42:43]
	s_mov_b32 m0, s24
	ds_read_b128 v[186:189], v224 offset:49152
	ds_read_b128 v[190:193], v224 offset:50176
	ds_read_b128 v[178:181], v224 offset:51200
	ds_read_b128 v[182:185], v224 offset:52224
	ds_read_b128 v[170:173], v224 offset:53248
	ds_read_b128 v[174:177], v224 offset:54272
	ds_read_b128 v[162:165], v224 offset:55296
	ds_read_b128 v[166:169], v224 offset:56320
	global_load_lds_dwordx4 v[214:215], off
	s_add_i32 m0, s24, 0x2000
	s_add_u32 s22, s22, 0x80080
	v_lshl_add_u64 v[214:215], v[216:217], 0, s[42:43]
	s_addc_u32 s23, s23, 0
	s_add_i32 s24, vcc_hi, s28
	global_load_lds_dwordx4 v[214:215], off
	v_lshl_add_u64 v[214:215], s[22:23], 0, v[200:201]
	s_mov_b32 m0, s24
	s_andn2_b64 vcc, exec, s[96:97]
	global_load_lds_dwordx4 v[214:215], off
	v_lshl_add_u64 v[214:215], s[22:23], 0, v[204:205]
	s_add_i32 m0, s24, 0x2000
	s_nop 0
	global_load_lds_dwordx4 v[214:215], off
	v_lshl_add_u64 v[214:215], v[218:219], 0, s[42:43]
	s_mov_b32 m0, s91
	s_nop 0
	global_load_lds_dwordx4 v[214:215], off
	v_lshl_add_u64 v[214:215], v[220:221], 0, s[42:43]
	s_mov_b32 m0, s94
	s_nop 0
	global_load_lds_dwordx4 v[214:215], off
	s_waitcnt vmcnt(8)
	s_waitcnt lgkmcnt(0)
	s_barrier
	s_cbranch_vccnz .LBB0_513
	s_waitcnt lgkmcnt(0)
	v_mfma_f32_16x16x32_bf16 v[60:63], v[146:149], v[186:189], v[60:63]
	v_mfma_f32_16x16x32_bf16 v[56:59], v[154:157], v[186:189], v[56:59]
	v_mfma_f32_16x16x32_bf16 v[44:47], v[146:149], v[178:181], v[44:47]
	v_mfma_f32_16x16x32_bf16 v[40:43], v[154:157], v[178:181], v[40:43]
	v_mfma_f32_16x16x32_bf16 v[28:31], v[146:149], v[170:173], v[28:31]
	v_mfma_f32_16x16x32_bf16 v[24:27], v[154:157], v[170:173], v[24:27]
	v_mfma_f32_16x16x32_bf16 v[12:15], v[146:149], v[162:165], v[12:15]
	v_mfma_f32_16x16x32_bf16 v[8:11], v[154:157], v[162:165], v[8:11]
	v_mfma_f32_16x16x32_bf16 v[60:63], v[150:153], v[190:193], v[60:63]
	v_mfma_f32_16x16x32_bf16 v[56:59], v[158:161], v[190:193], v[56:59]
	v_mfma_f32_16x16x32_bf16 v[44:47], v[150:153], v[182:185], v[44:47]
	v_mfma_f32_16x16x32_bf16 v[40:43], v[158:161], v[182:185], v[40:43]
	v_mfma_f32_16x16x32_bf16 v[28:31], v[150:153], v[174:177], v[28:31]
	v_mfma_f32_16x16x32_bf16 v[24:27], v[158:161], v[174:177], v[24:27]
	v_mfma_f32_16x16x32_bf16 v[12:15], v[150:153], v[166:169], v[12:15]
	v_mfma_f32_16x16x32_bf16 v[8:11], v[158:161], v[166:169], v[8:11]
	v_mfma_f32_16x16x32_bf16 v[52:55], v[130:133], v[186:189], v[52:55]
	v_mfma_f32_16x16x32_bf16 v[48:51], v[138:141], v[186:189], v[48:51]
	v_mfma_f32_16x16x32_bf16 v[36:39], v[130:133], v[178:181], v[36:39]
	v_mfma_f32_16x16x32_bf16 v[32:35], v[138:141], v[178:181], v[32:35]
	v_mfma_f32_16x16x32_bf16 v[20:23], v[130:133], v[170:173], v[20:23]
	v_mfma_f32_16x16x32_bf16 v[16:19], v[138:141], v[170:173], v[16:19]
	v_mfma_f32_16x16x32_bf16 v[4:7], v[130:133], v[162:165], v[4:7]
	v_mfma_f32_16x16x32_bf16 v[0:3], v[138:141], v[162:165], v[0:3]
	v_mfma_f32_16x16x32_bf16 v[52:55], v[134:137], v[190:193], v[52:55]
	v_mfma_f32_16x16x32_bf16 v[48:51], v[142:145], v[190:193], v[48:51]
	v_mfma_f32_16x16x32_bf16 v[36:39], v[134:137], v[182:185], v[36:39]
	v_mfma_f32_16x16x32_bf16 v[32:35], v[142:145], v[182:185], v[32:35]
	v_mfma_f32_16x16x32_bf16 v[20:23], v[134:137], v[174:177], v[20:23]
	v_mfma_f32_16x16x32_bf16 v[16:19], v[142:145], v[174:177], v[16:19]
	v_mfma_f32_16x16x32_bf16 v[4:7], v[134:137], v[166:169], v[4:7]
	v_mfma_f32_16x16x32_bf16 v[0:3], v[142:145], v[166:169], v[0:3]
	s_branch .LBB0_513
